# speedup vs baseline: 1.0145x; 1.0072x over previous
.LBB1_10:
	s_add_i32 s29, s28, 0x8000
	s_cmp_lg_u32 s28, 0x10000
	s_cselect_b32 s29, s29, 0
	s_add_i32 s36, s19, s29
	s_mov_b32 m0, s36
	s_nop 0
	global_load_lds_dwordx4 v199, s[16:17]
	s_add_i32 s34, s36, 0x400
	s_mov_b32 m0, s34
	s_nop 0
	global_load_lds_dwordx4 v208, s[16:17]
	s_add_u32 s34, s16, 0x2000
	s_addc_u32 s35, s17, 0
	s_add_i32 s37, s36, 0x2000
	s_mov_b32 m0, s37
	s_nop 0
	global_load_lds_dwordx4 v199, s[34:35]
	s_add_i32 s37, s36, 0x2400
	s_mov_b32 m0, s37
	s_nop 0
	global_load_lds_dwordx4 v208, s[34:35]
	s_add_u32 s34, s16, 0x4000
	s_addc_u32 s35, s17, 0
	s_add_i32 s37, s36, 0x4000
	s_mov_b32 m0, s37
	s_nop 0
	global_load_lds_dwordx4 v199, s[34:35]
	s_add_i32 s37, s36, 0x4400
	s_mov_b32 m0, s37
	s_nop 0
	global_load_lds_dwordx4 v208, s[34:35]
	s_add_u32 s16, s16, 0x6000
	s_addc_u32 s17, s17, 0
	s_add_i32 s34, s36, 0x6000
	s_mov_b32 m0, s34
	s_nop 0
	global_load_lds_dwordx4 v199, s[16:17]
	s_addk_i32 s36, 0x6400
	s_mov_b32 m0, s36
	s_nop 0
	global_load_lds_dwordx4 v208, s[16:17]
	s_andn2_b32 s16, 1, s33
	s_lshl_b32 s17, s16, 4
	s_add_i32 s17, s17, 0
	s_add_i32 s17, s17, s27
	s_add_i32 s17, s17, 0x20800
	v_mov_b32_e32 v213, s17
	ds_read_b64 v[214:215], v213
	s_waitcnt lgkmcnt(0)
	v_readfirstlane_b32 s17, v214
	s_cmp_eq_u32 s33, 1
	s_cbranch_scc1 .LBB1_14
	s_cmp_eq_u32 s17, 0
	v_readfirstlane_b32 s17, v215
	s_cbranch_scc1 .LBB1_12
	v_lshl_add_u32 v213, s16, 10, v210
	ds_read_b32 v214, v213
	s_waitcnt lgkmcnt(0)
	v_pk_mul_f32 v[126:127], v[214:215], v[126:127] op_sel_hi:[0,1]
	v_pk_mul_f32 v[124:125], v[214:215], v[124:125] op_sel_hi:[0,1]
	v_pk_mul_f32 v[122:123], v[214:215], v[122:123] op_sel_hi:[0,1]
	v_pk_mul_f32 v[120:121], v[214:215], v[120:121] op_sel_hi:[0,1]
	v_pk_mul_f32 v[118:119], v[214:215], v[118:119] op_sel_hi:[0,1]
	v_pk_mul_f32 v[116:117], v[214:215], v[116:117] op_sel_hi:[0,1]
	v_pk_mul_f32 v[114:115], v[214:215], v[114:115] op_sel_hi:[0,1]
	v_pk_mul_f32 v[112:113], v[214:215], v[112:113] op_sel_hi:[0,1]
	v_pk_mul_f32 v[94:95], v[214:215], v[94:95] op_sel_hi:[0,1]
	v_pk_mul_f32 v[92:93], v[214:215], v[92:93] op_sel_hi:[0,1]
	v_pk_mul_f32 v[90:91], v[214:215], v[90:91] op_sel_hi:[0,1]
	v_pk_mul_f32 v[88:89], v[214:215], v[88:89] op_sel_hi:[0,1]
	v_pk_mul_f32 v[86:87], v[214:215], v[86:87] op_sel_hi:[0,1]
	v_pk_mul_f32 v[84:85], v[214:215], v[84:85] op_sel_hi:[0,1]
	v_pk_mul_f32 v[82:83], v[214:215], v[82:83] op_sel_hi:[0,1]
	v_pk_mul_f32 v[80:81], v[214:215], v[80:81] op_sel_hi:[0,1]
	v_pk_mul_f32 v[62:63], v[214:215], v[62:63] op_sel_hi:[0,1]
	v_pk_mul_f32 v[60:61], v[214:215], v[60:61] op_sel_hi:[0,1]
	v_pk_mul_f32 v[58:59], v[214:215], v[58:59] op_sel_hi:[0,1]
	v_pk_mul_f32 v[56:57], v[214:215], v[56:57] op_sel_hi:[0,1]
	v_pk_mul_f32 v[54:55], v[214:215], v[54:55] op_sel_hi:[0,1]
	v_pk_mul_f32 v[52:53], v[214:215], v[52:53] op_sel_hi:[0,1]
	v_pk_mul_f32 v[50:51], v[214:215], v[50:51] op_sel_hi:[0,1]
	v_pk_mul_f32 v[48:49], v[214:215], v[48:49] op_sel_hi:[0,1]
	v_pk_mul_f32 v[14:15], v[214:215], v[14:15] op_sel_hi:[0,1]
	v_pk_mul_f32 v[12:13], v[214:215], v[12:13] op_sel_hi:[0,1]
	v_pk_mul_f32 v[10:11], v[214:215], v[10:11] op_sel_hi:[0,1]
	v_pk_mul_f32 v[8:9], v[214:215], v[8:9] op_sel_hi:[0,1]
	v_pk_mul_f32 v[6:7], v[214:215], v[6:7] op_sel_hi:[0,1]
	v_pk_mul_f32 v[4:5], v[214:215], v[4:5] op_sel_hi:[0,1]
	v_pk_mul_f32 v[2:3], v[214:215], v[2:3] op_sel_hi:[0,1]
	v_pk_mul_f32 v[0:1], v[214:215], v[0:1] op_sel_hi:[0,1]

.LBB1_20:
	v_exp_f32_e32 v16, v16
	s_lshl_b32 s15, s13, 4
	v_exp_f32_e32 v17, v17
	s_add_i32 s15, s10, s15
	v_exp_f32_e32 v18, v18
	v_mov_b32_e32 v91, s15
	v_mov_b32_e32 v92, s14
	v_exp_f32_e32 v19, v19
	ds_write_b32 v91, v92
	v_add_f32_e32 v91, 0, v16
	v_exp_f32_e32 v20, v20
	v_add_f32_e32 v91, v91, v17
	v_exp_f32_e32 v21, v21
	v_add_f32_e32 v91, v91, v18
	v_exp_f32_e32 v22, v22
	v_add_f32_e32 v91, v91, v19
	v_exp_f32_e32 v23, v23
	v_add_f32_e32 v91, v91, v20
	v_exp_f32_e32 v24, v24
	v_add_f32_e32 v91, v91, v21
	v_exp_f32_e32 v25, v25
	v_add_f32_e32 v91, v91, v22
	v_exp_f32_e32 v26, v26
	v_add_f32_e32 v91, v91, v23
	v_exp_f32_e32 v27, v27
	v_add_f32_e32 v91, v91, v24
	v_exp_f32_e32 v28, v28
	v_add_f32_e32 v91, v91, v25
	v_exp_f32_e32 v29, v29
	v_add_f32_e32 v91, v91, v26
	v_exp_f32_e32 v30, v30
	v_add_f32_e32 v91, v91, v27
	v_exp_f32_e32 v31, v31
	v_add_f32_e32 v91, v91, v28
	v_exp_f32_e32 v32, v32
	v_add_f32_e32 v91, v91, v29
	v_exp_f32_e32 v33, v33
	v_add_f32_e32 v91, v91, v30
	v_exp_f32_e32 v34, v34
	v_add_f32_e32 v91, v91, v31
	v_exp_f32_e32 v35, v35
	v_add_f32_e32 v91, v91, v32
	v_exp_f32_e32 v36, v36
	v_add_f32_e32 v91, v91, v33
	v_exp_f32_e32 v37, v37
	v_add_f32_e32 v91, v91, v34
	v_exp_f32_e32 v38, v38
	v_add_f32_e32 v91, v91, v35
	v_exp_f32_e32 v39, v39
	v_add_f32_e32 v91, v91, v36
	v_exp_f32_e32 v40, v40
	v_add_f32_e32 v91, v91, v37
	v_exp_f32_e32 v41, v41
	v_add_f32_e32 v91, v91, v38
	v_exp_f32_e32 v42, v42
	v_add_f32_e32 v91, v91, v39
	v_exp_f32_e32 v43, v43
	v_add_f32_e32 v91, v91, v40
	v_exp_f32_e32 v44, v44
	v_add_f32_e32 v91, v91, v41
	v_exp_f32_e32 v45, v45
	v_add_f32_e32 v91, v91, v42
	v_exp_f32_e32 v46, v46
	v_add_f32_e32 v91, v91, v43
	v_exp_f32_e32 v47, v47
	v_add_f32_e32 v91, v91, v44
	v_add_f32_e32 v91, v91, v45
	v_add_f32_e32 v91, v91, v46
	v_add_f32_e32 v91, v91, v47
	v_add_f32_e32 v99, v99, v91
	v_lshl_add_u32 v91, s13, 14, v89
	v_cvt_pk_bf16_f32 v16, v16, v17
	v_cvt_pk_bf16_f32 v17, v18, v19
	v_cvt_pk_bf16_f32 v18, v20, v21
	v_cvt_pk_bf16_f32 v19, v22, v23
	ds_write_b128 v91, v[16:19]
	v_cvt_pk_bf16_f32 v16, v24, v25
	v_cvt_pk_bf16_f32 v17, v26, v27
	v_cvt_pk_bf16_f32 v18, v28, v29
	v_cvt_pk_bf16_f32 v19, v30, v31
	ds_write_b128 v91, v[16:19] offset:1024
	v_cvt_pk_bf16_f32 v16, v32, v33
	v_cvt_pk_bf16_f32 v17, v34, v35
	v_cvt_pk_bf16_f32 v18, v36, v37
	v_cvt_pk_bf16_f32 v19, v38, v39
	ds_write_b128 v91, v[16:19] offset:2048
	v_cvt_pk_bf16_f32 v16, v40, v41
	v_cvt_pk_bf16_f32 v17, v42, v43
	v_cvt_pk_bf16_f32 v18, v44, v45
	v_cvt_pk_bf16_f32 v19, v46, v47
	ds_write_b128 v91, v[16:19] offset:3072
	s_add_i32 s13, s5, 0x8000
	s_cmp_lg_u32 s5, 0x10000
	s_cselect_b32 s5, s13, 0
	s_add_i32 s11, s11, 1
	s_cmp_eq_u32 s11, 16
	s_waitcnt lgkmcnt(0)
	s_barrier
	s_cbranch_scc1 .LBB1_23
